# also the P2-end drain loop: counted vmcnt waits (all four weight-converter drain loops now overlap the next load batch)
# baseline (speedup 1.0000x reference)
;     __device__ __forceinline__ CvtDesc desc(int qq) const { return cvt_desc(*F, item_of(qq), qq & 1, h); }
;     __device__ __forceinline__ void proc() { cvt_to_lds(buf, desc(q), img, gl, q & 1, h, F->lane); if (q & 1) fitem = item_of(q); ++q; }
;     __device__ __forceinline__ void flush() { if (fitem >= 0) { cvt_flush(cvt_desc(*F, fitem, 0, h), img, h, F->lane); fitem = -1; } }
;     __device__ __forceinline__ void drain() {
;         __syncthreads(); flush(); __syncthreads();
;         if (state != 0) { proc(); state = 0; if (fitem >= 0) { __syncthreads(); flush(); __syncthreads(); } }
;         if (q >= nq) { __syncthreads(); return; }
;         CvtBuf b2;
;         cvt_load(buf, desc(q), F->lane);
;         while (q < nq) {
;             if (q + 1 < nq) cvt_load(b2, desc(q + 1), F->lane);
;             cvt_to_lds(buf, desc(q), img, gl, q & 1, h, F->lane); if (q & 1) fitem = item_of(q); ++q;
;             if (fitem >= 0) { __syncthreads(); flush(); __syncthreads(); }
;             if (q >= nq) break;
;             if (q + 1 < nq) cvt_load(buf, desc(q + 1), F->lane);
;             cvt_to_lds(b2, desc(q), img, gl, q & 1, h, F->lane); if (q & 1) fitem = item_of(q); ++q;
.LBB0_689:
	s_add_i32 s40, s10, 1
	s_cmp_lt_i32 s40, s54
	s_cselect_b64 s[8:9], -1, 0
	s_cmp_ge_i32 s40, s54
	s_cbranch_scc0 .Ldr2_goA
	s_waitcnt vmcnt(0)
	s_branch .LBB0_695
.Ldr2_goA:
	s_ashr_i32 s0, s40, 1
	s_mul_i32 s41, s0, s55
	s_add_i32 s41, s41, s3
	s_cmpk_gt_i32 s41, 0x3fff
	s_mov_b64 s[14:15], -1
	s_cbranch_scc0 .LBB0_692
	s_add_i32 s0, s41, 0xffffc000
	s_lshr_b32 s4, s0, 8
	v_readlane_b32 s12, v254, 0
	s_lshr_b32 s36, s41, 4
	s_and_b32 s37, s41, 15
	s_lshl_b64 s[0:1], s[4:5], 24
	v_readlane_b32 s14, v254, 2
	v_readlane_b32 s15, v254, 3
	s_add_u32 s0, s14, s0
	v_readlane_b32 s13, v254, 1
	v_readlane_b32 s16, v254, 4
	v_readlane_b32 s17, v254, 5
	v_readlane_b32 s18, v254, 6
	v_readlane_b32 s19, v254, 7
	s_addc_u32 s1, s15, s1
	s_mov_b64 s[14:15], 0

; #define LAS __attribute__((address_space(3)))
; __device__ __forceinline__ unsigned pk4_fp8(float a, float b, float c, float d) { int w = __builtin_amdgcn_cvt_pk_fp8_f32(a, b, 0, false); w = __builtin_amdgcn_cvt_pk_fp8_f32(c, d, w, true); return (unsigned)w; }
;     __device__ __forceinline__ CvtDesc desc(int qq) const { return cvt_desc(*F, item_of(qq), qq & 1, h); }
; __device__ __forceinline__ void cvt_to_lds(const CvtBuf& b, const CvtDesc& d, LAS unsigned char* img, const LAS float* gl, int sub2, int h, int lane) {
;     const int hh = lane >> 5, l5 = lane & 31;
;     float gs[16];
;     const bool use_g = d.map == 2;
; #pragma unroll
;     for (int q = 0; q < 4; ++q) { const f32x4 gv = *(const LAS f32x4*)(gl + d.k0 + 16 * hh + 4 * q);
; #pragma unroll
;         for (int j = 0; j < 4; ++j) gs[4 * q + j] = use_g ? gv[j] : WSCALE; }
;     const int c8 = 4 * h + 2 * sub2 + hh;
; #pragma unroll
;     for (int j = 0; j < 4; ++j) { u32x4 o;
; #pragma unroll
;         for (int q = 0; q < 4; ++q) { const int i = 4 * q; o[q] = pk4_fp8(b.v[i][j] * gs[i], b.v[i + 1][j] * gs[i + 1], b.v[i + 2][j] * gs[i + 2], b.v[i + 3][j] * gs[i + 3]); }
;         *(LAS u32x4*)(img + (4 * l5 + j) * 128 + 16 * (c8 ^ (l5 & 7))) = o; }
; }
;     __device__ __forceinline__ void proc() { cvt_to_lds(buf, desc(q), img, gl, q & 1, h, F->lane); if (q & 1) fitem = item_of(q); ++q; }
.LBB0_695:
	s_ashr_i32 s0, s10, 1
	s_mul_i32 s0, s0, s55
	s_add_i32 s0, s0, s3
	s_cmpk_lt_i32 s0, 0x4000
	s_cselect_b64 vcc, -1, 0
	s_and_b64 s[14:15], vcc, exec
	s_cselect_b32 s1, 5, 4
	s_lshr_b32 s1, s0, s1
	s_lshl_b32 s4, s10, 5
	s_lshl_b32 s1, s1, 9
	s_and_b32 s41, s4, 32
	s_and_b32 s1, s1, 0x1e00
	s_add_i32 s1, s11, s1
	s_lshl_b32 s4, s41, 2
	s_add_i32 s1, s1, s4
	v_add_u32_e32 v130, s1, v133
	ds_read_b128 v[152:155], v130 offset:49152
	ds_read_b128 v[156:159], v130 offset:49168
	ds_read_b128 v[160:163], v130 offset:49184
	ds_read_b128 v[164:167], v130 offset:49200
	s_lshl_b32 s1, s10, 1
	s_waitcnt lgkmcnt(3)
	v_cndmask_b32_e32 v130, v151, v152, vcc
	v_cndmask_b32_e32 v136, v151, v153, vcc
	v_cndmask_b32_e32 v137, v151, v154, vcc
	s_waitcnt lgkmcnt(2)
	v_cndmask_b32_e32 v169, v151, v156, vcc
	v_cndmask_b32_e32 v170, v151, v157, vcc
	s_waitcnt vmcnt(31)
	v_mul_f32_e32 v153, v2, v130
	s_waitcnt vmcnt(30)
	v_mul_f32_e32 v154, v6, v136
	v_mov_b32_e32 v152, v131
	v_cvt_pk_fp8_f32 v152, v153, v154
	s_waitcnt vmcnt(27)
	v_mul_f32_e32 v154, v18, v169
	s_waitcnt vmcnt(26)
	v_mul_f32_e32 v157, v22, v170
	v_mov_b32_e32 v153, v131
	v_cvt_pk_fp8_f32 v153, v154, v157
	v_cndmask_b32_e32 v168, v151, v155, vcc
	v_cndmask_b32_e32 v171, v151, v158, vcc
	v_cndmask_b32_e32 v172, v151, v159, vcc
	v_mul_f32_e32 v155, v10, v137
	v_mul_f32_e32 v156, v14, v168
	s_waitcnt lgkmcnt(1)
	v_cndmask_b32_e32 v173, v151, v160, vcc
	v_cndmask_b32_e32 v174, v151, v161, vcc
	v_cvt_pk_fp8_f32 v152, v155, v156 op_sel:[0,0,1]
	s_waitcnt vmcnt(25)
	v_mul_f32_e32 v154, v26, v171
	s_waitcnt vmcnt(24)
	v_mul_f32_e32 v155, v30, v172
	s_waitcnt lgkmcnt(0)
	v_cndmask_b32_e32 v164, v151, v164, vcc
	v_cndmask_b32_e32 v165, v151, v165, vcc
	v_cvt_pk_fp8_f32 v153, v154, v155 op_sel:[0,0,1]
	s_waitcnt vmcnt(23)
	v_mul_f32_e32 v155, v34, v173
	s_waitcnt vmcnt(22)
	v_mul_f32_e32 v156, v38, v174
	v_mov_b32_e32 v154, v131
	v_cvt_pk_fp8_f32 v154, v155, v156
	s_waitcnt vmcnt(19)
	v_mul_f32_e32 v156, v50, v164
	s_waitcnt vmcnt(18)
	v_mul_f32_e32 v159, v54, v165
	v_mov_b32_e32 v155, v131
	v_cvt_pk_fp8_f32 v155, v156, v159
	v_cndmask_b32_e32 v175, v151, v162, vcc
	v_cndmask_b32_e32 v176, v151, v163, vcc
	v_cndmask_b32_e32 v166, v151, v166, vcc
	v_cndmask_b32_e32 v167, v151, v167, vcc
	v_mul_f32_e32 v157, v42, v175
	v_mul_f32_e32 v158, v46, v176
	v_cvt_pk_fp8_f32 v154, v157, v158 op_sel:[0,0,1]
	s_waitcnt vmcnt(17)
	v_mul_f32_e32 v156, v58, v166
	s_waitcnt vmcnt(16)
	v_mul_f32_e32 v157, v62, v167
	v_cvt_pk_fp8_f32 v155, v156, v157 op_sel:[0,0,1]
	v_mul_f32_e32 v157, v3, v130
	v_mul_f32_e32 v158, v7, v136
	v_mov_b32_e32 v156, v131
	v_cvt_pk_fp8_f32 v156, v157, v158
	v_mul_f32_e32 v158, v19, v169
	v_mul_f32_e32 v161, v23, v170
	v_mov_b32_e32 v157, v131
	v_cvt_pk_fp8_f32 v157, v158, v161
	v_mul_f32_e32 v159, v11, v137
	v_mul_f32_e32 v160, v15, v168
	v_cvt_pk_fp8_f32 v156, v159, v160 op_sel:[0,0,1]
	v_mul_f32_e32 v158, v27, v171
	v_mul_f32_e32 v159, v31, v172
	v_cvt_pk_fp8_f32 v157, v158, v159 op_sel:[0,0,1]
	v_mul_f32_e32 v159, v35, v173
	v_mul_f32_e32 v160, v39, v174
	v_mov_b32_e32 v158, v131
	v_cvt_pk_fp8_f32 v158, v159, v160
	v_mul_f32_e32 v160, v51, v164
	v_mul_f32_e32 v163, v55, v165
	v_mov_b32_e32 v159, v131
	v_cvt_pk_fp8_f32 v159, v160, v163
	v_mul_f32_e32 v161, v43, v175
	v_mul_f32_e32 v162, v47, v176
	v_cvt_pk_fp8_f32 v158, v161, v162 op_sel:[0,0,1]
	v_mul_f32_e32 v160, v59, v166
	v_mul_f32_e32 v161, v63, v167
	v_cvt_pk_fp8_f32 v159, v160, v161 op_sel:[0,0,1]
	v_mul_f32_e32 v161, v4, v130
	v_mul_f32_e32 v162, v8, v136
	v_mov_b32_e32 v160, v131
	v_cvt_pk_fp8_f32 v160, v161, v162
	v_mul_f32_e32 v162, v20, v169
	v_mul_f32_e32 v179, v24, v170
	v_mov_b32_e32 v161, v131
	v_cvt_pk_fp8_f32 v161, v162, v179
	v_mul_f32_e32 v163, v12, v137
	v_mul_f32_e32 v178, v16, v168
	v_cvt_pk_fp8_f32 v160, v163, v178 op_sel:[0,0,1]
	v_mul_f32_e32 v162, v28, v171
	v_mul_f32_e32 v163, v32, v172
	v_cvt_pk_fp8_f32 v161, v162, v163 op_sel:[0,0,1]
	v_mul_f32_e32 v163, v36, v173
	v_mul_f32_e32 v178, v40, v174
	v_mov_b32_e32 v162, v131
	v_cvt_pk_fp8_f32 v162, v163, v178
	v_mul_f32_e32 v178, v52, v164
	v_mul_f32_e32 v181, v56, v165
	v_mov_b32_e32 v163, v131
	v_cvt_pk_fp8_f32 v163, v178, v181
	v_mul_f32_e32 v179, v44, v175
	v_mul_f32_e32 v180, v48, v176
	s_and_b32 s1, s1, 2
	v_cvt_pk_fp8_f32 v162, v179, v180 op_sel:[0,0,1]
	v_mul_f32_e32 v178, v60, v166
	v_mul_f32_e32 v179, v64, v167
	v_bitop3_b32 v177, s1, v139, v141 bitop3:0x36
	v_cvt_pk_fp8_f32 v163, v178, v179 op_sel:[0,0,1]
	v_lshl_add_u32 v177, v177, 4, v138
	ds_write_b128 v177, v[152:155]
	ds_write_b128 v177, v[156:159] offset:128
	ds_write_b128 v177, v[160:163] offset:256
	v_mul_f32_e32 v130, v5, v130
	v_mul_f32_e32 v136, v9, v136
	v_mov_b32_e32 v152, v131
	v_cvt_pk_fp8_f32 v152, v130, v136
	v_mul_f32_e32 v130, v21, v169
	v_mul_f32_e32 v136, v25, v170
	v_mov_b32_e32 v153, v131
	v_cvt_pk_fp8_f32 v153, v130, v136
	v_mul_f32_e32 v137, v13, v137
	v_mul_f32_e32 v154, v17, v168
	v_mul_f32_e32 v130, v29, v171
	v_mul_f32_e32 v136, v33, v172
	v_cvt_pk_fp8_f32 v152, v137, v154 op_sel:[0,0,1]
	v_cvt_pk_fp8_f32 v153, v130, v136 op_sel:[0,0,1]
	v_mul_f32_e32 v130, v37, v173
	v_mul_f32_e32 v136, v41, v174
	v_mov_b32_e32 v154, v131
	v_cvt_pk_fp8_f32 v154, v130, v136
	v_mul_f32_e32 v130, v53, v164
	v_mul_f32_e32 v136, v57, v165
	v_mov_b32_e32 v155, v131
	v_cvt_pk_fp8_f32 v155, v130, v136
	v_mul_f32_e32 v137, v45, v175
	v_mul_f32_e32 v156, v49, v176
	v_mul_f32_e32 v130, v61, v166
	v_mul_f32_e32 v136, v65, v167
	v_cvt_pk_fp8_f32 v154, v137, v156 op_sel:[0,0,1]
	v_cvt_pk_fp8_f32 v155, v130, v136 op_sel:[0,0,1]
	s_and_b64 s[14:15], s[6:7], exec
	s_cselect_b32 s42, s61, s0
	s_cmp_lt_i32 s42, 0
	ds_write_b128 v177, v[152:155] offset:384
	s_cbranch_scc1 .LBB0_703
	s_cmpk_lt_u32 s42, 0x4000
	s_cselect_b64 s[0:1], -1, 0
	s_cmpk_gt_u32 s42, 0x3fff
	s_mov_b64 s[36:37], -1
	s_waitcnt lgkmcnt(0)
	s_barrier
	s_cbranch_scc0 .LBB0_698
	s_add_i32 s4, s42, 0xffffc000
	s_lshr_b32 s4, s4, 8
	s_lshr_b32 s43, s42, 4
	s_and_b32 s44, s42, 15
	s_lshl_b64 s[14:15], s[4:5], 22
	s_add_u32 s14, s34, s14
	s_addc_u32 s15, s35, s15
	s_mov_b64 s[36:37], 0

;     __device__ __forceinline__ CvtDesc desc(int qq) const { return cvt_desc(*F, item_of(qq), qq & 1, h); }
;     __device__ __forceinline__ void flush() { if (fitem >= 0) { cvt_flush(cvt_desc(*F, fitem, 0, h), img, h, F->lane); fitem = -1; } }
;     __device__ __forceinline__ void drain() {
;     ...
;         while (q < nq) {
;             if (q + 1 < nq) cvt_load(b2, desc(q + 1), F->lane);
;             cvt_to_lds(buf, desc(q), img, gl, q & 1, h, F->lane); if (q & 1) fitem = item_of(q); ++q;
;             if (fitem >= 0) { __syncthreads(); flush(); __syncthreads(); }
;             if (q >= nq) break;
;             if (q + 1 < nq) cvt_load(buf, desc(q + 1), F->lane);
.LBB0_703:
	s_andn2_b64 vcc, exec, s[8:9]
	s_mov_b64 s[8:9], -1
	s_cbranch_vccnz .LBB0_688
	s_add_i32 s10, s10, 2
	s_cmp_ge_i32 s10, s54
	s_cselect_b64 s[8:9], -1, 0
	s_and_b64 vcc, exec, s[8:9]
	s_cbranch_vccz .Ldr2_goB
	s_waitcnt vmcnt(0)
	s_branch .LBB0_710
.Ldr2_goB:
	s_ashr_i32 s0, s10, 1
	s_mul_i32 s43, s0, s55
	s_add_i32 s43, s43, s3
	s_cmpk_gt_i32 s43, 0x3fff
	s_mov_b64 s[14:15], -1
	s_cbranch_scc0 .LBB0_707
	s_add_i32 s0, s43, 0xffffc000
	s_lshr_b32 s4, s0, 8
	v_readlane_b32 s12, v254, 0
	s_lshr_b32 s36, s43, 4
	s_and_b32 s37, s43, 15
	s_lshl_b64 s[0:1], s[4:5], 24
	v_readlane_b32 s14, v254, 2
	v_readlane_b32 s15, v254, 3
	s_add_u32 s0, s14, s0
	v_readlane_b32 s13, v254, 1
	v_readlane_b32 s16, v254, 4
	v_readlane_b32 s17, v254, 5
	v_readlane_b32 s18, v254, 6
	v_readlane_b32 s19, v254, 7
	s_addc_u32 s1, s15, s1
	s_mov_b64 s[14:15], 0

;     __device__ __forceinline__ CvtDesc desc(int qq) const { return cvt_desc(*F, item_of(qq), qq & 1, h); }
; __device__ __forceinline__ void cvt_load(CvtBuf& b, const CvtDesc& d, int lane) {
;     const float* p = d.W + (size_t)(d.k0 + 16 * (lane >> 5)) * d.ldw + d.n0 + 4 * (lane & 31);
; #pragma unroll
;     for (int i = 0; i < 16; ++i) b.v[i] = __builtin_nontemporal_load((const f32x4*)(p + (size_t)i * d.ldw));
; }
;     __device__ __forceinline__ void drain() {
;     ...
;             if (q + 1 < nq) cvt_load(buf, desc(q + 1), F->lane);
;             cvt_to_lds(b2, desc(q), img, gl, q & 1, h, F->lane); if (q & 1) fitem = item_of(q); ++q;
.LBB0_709:
	s_lshl_b32 s15, s36, 7
	s_and_b32 s15, s15, 0x780
	v_or_b32_e32 v2, s15, v1
	v_or_b32_e32 v2, s41, v2
	v_mul_u32_u24_e32 v2, s14, v2
	v_lshlrev_b32_e32 v130, 2, v2
	s_lshl_b32 s4, s37, 7
	v_lshl_add_u64 v[2:3], s[0:1], 0, v[130:131]
	v_lshl_add_u64 v[2:3], s[4:5], 2, v[2:3]
	v_lshlrev_b32_e32 v130, 2, v132
	v_lshl_add_u64 v[2:3], v[2:3], 0, v[130:131]
	s_lshl_b32 s4, s14, 2
	v_lshl_add_u64 v[10:11], v[2:3], 0, s[4:5]
	global_load_dwordx4 v[2:5], v[2:3], off nt
	s_nop 0
	global_load_dwordx4 v[6:9], v[10:11], off nt
	v_lshl_add_u64 v[10:11], v[10:11], 0, s[4:5]
	v_lshl_add_u64 v[18:19], v[10:11], 0, s[4:5]
	global_load_dwordx4 v[10:13], v[10:11], off nt
	s_nop 0
	global_load_dwordx4 v[14:17], v[18:19], off nt
	v_lshl_add_u64 v[18:19], v[18:19], 0, s[4:5]
	v_lshl_add_u64 v[26:27], v[18:19], 0, s[4:5]
	global_load_dwordx4 v[18:21], v[18:19], off nt
	s_nop 0
	global_load_dwordx4 v[22:25], v[26:27], off nt
	v_lshl_add_u64 v[26:27], v[26:27], 0, s[4:5]
	v_lshl_add_u64 v[34:35], v[26:27], 0, s[4:5]
	v_lshl_add_u64 v[38:39], v[34:35], 0, s[4:5]
	v_lshl_add_u64 v[42:43], v[38:39], 0, s[4:5]
	v_lshl_add_u64 v[46:47], v[42:43], 0, s[4:5]
	v_lshl_add_u64 v[50:51], v[46:47], 0, s[4:5]
	v_lshl_add_u64 v[54:55], v[50:51], 0, s[4:5]
	v_lshl_add_u64 v[58:59], v[54:55], 0, s[4:5]
	v_lshl_add_u64 v[62:63], v[58:59], 0, s[4:5]
	global_load_dwordx4 v[26:29], v[26:27], off nt
	s_nop 0
	global_load_dwordx4 v[30:33], v[34:35], off nt
	s_nop 0
	global_load_dwordx4 v[34:37], v[38:39], off nt
	s_nop 0
	global_load_dwordx4 v[38:41], v[42:43], off nt
	s_nop 0
	global_load_dwordx4 v[42:45], v[46:47], off nt
	s_nop 0
	global_load_dwordx4 v[46:49], v[50:51], off nt
	s_nop 0
	global_load_dwordx4 v[50:53], v[54:55], off nt
	s_nop 0
	global_load_dwordx4 v[54:57], v[58:59], off nt
	s_nop 0
	global_load_dwordx4 v[58:61], v[62:63], off nt
	v_lshl_add_u64 v[62:63], v[62:63], 0, s[4:5]
	global_load_dwordx4 v[62:65], v[62:63], off nt
	s_waitcnt vmcnt(16)
